# speedup vs baseline: 1.0103x; 1.0103x over previous
.LBB5_140:
	v_lshl_or_b32 v2, s42, 3, v187
	v_ashrrev_i32_e32 v3, 31, v2
	v_lshlrev_b64 v[2:3], 16, v[2:3]
	v_lshl_add_u64 v[2:3], s[48:49], 0, v[2:3]
	v_mov_b32_e32 v169, 0
	v_lshlrev_b32_e32 v168, 4, v189
	s_or_b32 s25, s2, s50
	s_or_b32 s24, s50, 1
	s_mov_b32 s1, 0
	v_lshl_add_u64 v[166:167], v[2:3], 0, v[168:169]
	s_lshl_b32 s0, s25, 12
	s_or_b32 s30, s2, s24
	v_lshl_add_u64 v[18:19], v[166:167], 0, s[0:1]
	s_lshl_b32 s0, s30, 12
	v_lshl_add_u64 v[34:35], v[166:167], 0, s[0:1]
	global_load_dwordx4 v[2:5], v[18:19], off
	global_load_dwordx4 v[6:9], v[18:19], off offset:1024
	global_load_dwordx4 v[10:13], v[18:19], off offset:2048
	global_load_dwordx4 v[14:17], v[18:19], off offset:3072
	s_nop 0
	global_load_dwordx4 v[18:21], v[34:35], off
	global_load_dwordx4 v[22:25], v[34:35], off offset:1024
	global_load_dwordx4 v[26:29], v[34:35], off offset:2048
	global_load_dwordx4 v[30:33], v[34:35], off offset:3072
	v_or_b32_e32 v52, v147, v146
	s_add_i32 s0, s59, 2
	s_and_b32 s28, s0, 6
	s_or_b32 s31, s2, s28
	s_lshl_b32 s0, s31, 12
	v_lshl_add_u64 v[50:51], v[166:167], 0, s[0:1]
	s_waitcnt lgkmcnt(0)
	s_barrier
	global_load_dwordx4 v[34:37], v[50:51], off
	global_load_dwordx4 v[38:41], v[50:51], off offset:1024
	global_load_dwordx4 v[42:45], v[50:51], off offset:2048
	global_load_dwordx4 v[46:49], v[50:51], off offset:3072
	v_xad_u32 v191, v52, v152, 0
	v_lshl_add_u32 v122, s25, 10, v191
	ds_read_b128 v[50:53], v122
	ds_read_b128 v[54:57], v122 offset:16384
	ds_read_b128 v[58:61], v122 offset:32768
	ds_read_b128 v[62:65], v122 offset:49152
	s_setprio 1
	s_waitcnt vmcnt(11) lgkmcnt(3)
	v_mfma_f32_16x16x32_f16 v[66:69], v[2:5], v[50:53], 0
	s_waitcnt vmcnt(10)
	v_mfma_f32_16x16x32_f16 v[70:73], v[6:9], v[50:53], 0
	s_waitcnt vmcnt(9)
	v_mfma_f32_16x16x32_f16 v[74:77], v[10:13], v[50:53], 0
	s_waitcnt vmcnt(8)
	v_mfma_f32_16x16x32_f16 v[50:53], v[14:17], v[50:53], 0
	s_waitcnt lgkmcnt(2)
	v_mfma_f32_16x16x32_f16 v[78:81], v[2:5], v[54:57], 0
	v_mfma_f32_16x16x32_f16 v[82:85], v[6:9], v[54:57], 0
	v_mfma_f32_16x16x32_f16 v[86:89], v[10:13], v[54:57], 0
	v_mfma_f32_16x16x32_f16 v[54:57], v[14:17], v[54:57], 0
	s_waitcnt lgkmcnt(1)
	v_mfma_f32_16x16x32_f16 v[90:93], v[2:5], v[58:61], 0
	v_mfma_f32_16x16x32_f16 v[94:97], v[6:9], v[58:61], 0
	v_mfma_f32_16x16x32_f16 v[98:101], v[10:13], v[58:61], 0
	v_mfma_f32_16x16x32_f16 v[58:61], v[14:17], v[58:61], 0
	s_waitcnt lgkmcnt(0)
	v_mfma_f32_16x16x32_f16 v[102:105], v[2:5], v[62:65], 0
	v_mfma_f32_16x16x32_f16 v[106:109], v[6:9], v[62:65], 0
	v_mfma_f32_16x16x32_f16 v[110:113], v[10:13], v[62:65], 0
	v_mfma_f32_16x16x32_f16 v[62:65], v[14:17], v[62:65], 0
	s_setprio 0
	v_add_u32_e32 v114, 0x10000, v122
	v_add_u32_e32 v118, 0x14000, v122
	v_add_u32_e32 v123, 0x18000, v122
	v_add_u32_e32 v126, 0x1c000, v122
	ds_read_b128 v[114:117], v114
	ds_read_b128 v[118:121], v118
	ds_read_b128 v[122:125], v123
	ds_read_b128 v[126:129], v126
	s_setprio 1
	s_waitcnt lgkmcnt(3)
	v_mfma_f32_16x16x32_f16 v[130:133], v[2:5], v[114:117], 0
	v_mfma_f32_16x16x32_f16 v[134:137], v[6:9], v[114:117], 0
	v_mfma_f32_16x16x32_f16 v[138:141], v[10:13], v[114:117], 0
	v_mfma_f32_16x16x32_f16 v[114:117], v[14:17], v[114:117], 0
	s_waitcnt lgkmcnt(2)
	v_mfma_f32_16x16x32_f16 v[142:145], v[2:5], v[118:121], 0
	v_mfma_f32_16x16x32_f16 v[146:149], v[6:9], v[118:121], 0
	v_mfma_f32_16x16x32_f16 v[150:153], v[10:13], v[118:121], 0
	v_mfma_f32_16x16x32_f16 v[118:121], v[14:17], v[118:121], 0
	s_waitcnt lgkmcnt(1)
	v_mfma_f32_16x16x32_f16 v[154:157], v[2:5], v[122:125], 0
	v_mfma_f32_16x16x32_f16 v[158:161], v[6:9], v[122:125], 0
	v_mfma_f32_16x16x32_f16 v[170:173], v[10:13], v[122:125], 0
	v_mfma_f32_16x16x32_f16 v[122:125], v[14:17], v[122:125], 0
	s_waitcnt lgkmcnt(0)
	v_mfma_f32_16x16x32_f16 v[2:5], v[2:5], v[126:129], 0
	v_mfma_f32_16x16x32_f16 v[6:9], v[6:9], v[126:129], 0
	v_mfma_f32_16x16x32_f16 v[10:13], v[10:13], v[126:129], 0
	v_mfma_f32_16x16x32_f16 v[14:17], v[14:17], v[126:129], 0
	s_setprio 0
	s_add_i32 s0, s50, 3
	s_and_b32 s29, s0, 7
	s_or_b32 s48, s29, s2
	s_lshl_b32 s0, s48, 12
	v_lshl_add_u64 v[178:179], v[166:167], 0, s[0:1]
	global_load_dwordx4 v[126:129], v[178:179], off
	global_load_dwordx4 v[174:177], v[178:179], off offset:1024
	global_load_dwordx4 v[192:195], v[178:179], off offset:2048
	global_load_dwordx4 v[196:199], v[178:179], off offset:3072
	v_lshl_add_u32 v163, s30, 10, v191
	ds_read_b128 v[200:203], v163
	ds_read_b128 v[204:207], v163 offset:16384
	ds_read_b128 v[208:211], v163 offset:32768
	ds_read_b128 v[212:215], v163 offset:49152
	s_setprio 1
	s_waitcnt vmcnt(11) lgkmcnt(3)
	v_mfma_f32_16x16x32_f16 v[66:69], v[18:21], v[200:203], v[66:69]
	s_waitcnt vmcnt(10)
	v_mfma_f32_16x16x32_f16 v[70:73], v[22:25], v[200:203], v[70:73]
	s_waitcnt vmcnt(9)
	v_mfma_f32_16x16x32_f16 v[74:77], v[26:29], v[200:203], v[74:77]
	s_waitcnt vmcnt(8)
	v_mfma_f32_16x16x32_f16 v[50:53], v[30:33], v[200:203], v[50:53]
	s_waitcnt lgkmcnt(2)
	v_mfma_f32_16x16x32_f16 v[78:81], v[18:21], v[204:207], v[78:81]
	v_mfma_f32_16x16x32_f16 v[82:85], v[22:25], v[204:207], v[82:85]
	v_mfma_f32_16x16x32_f16 v[86:89], v[26:29], v[204:207], v[86:89]
	v_mfma_f32_16x16x32_f16 v[54:57], v[30:33], v[204:207], v[54:57]
	s_waitcnt lgkmcnt(1)
	v_mfma_f32_16x16x32_f16 v[90:93], v[18:21], v[208:211], v[90:93]
	v_mfma_f32_16x16x32_f16 v[94:97], v[22:25], v[208:211], v[94:97]
	v_mfma_f32_16x16x32_f16 v[98:101], v[26:29], v[208:211], v[98:101]
	v_mfma_f32_16x16x32_f16 v[58:61], v[30:33], v[208:211], v[58:61]
	s_waitcnt lgkmcnt(0)
	v_mfma_f32_16x16x32_f16 v[102:105], v[18:21], v[212:215], v[102:105]
	v_mfma_f32_16x16x32_f16 v[106:109], v[22:25], v[212:215], v[106:109]
	v_mfma_f32_16x16x32_f16 v[110:113], v[26:29], v[212:215], v[110:113]
	v_mfma_f32_16x16x32_f16 v[62:65], v[30:33], v[212:215], v[62:65]
	s_setprio 0
	v_add_u32_e32 v165, 0x10000, v163
	v_add_u32_e32 v168, 0x14000, v163
	ds_read_b128 v[200:203], v165
	ds_read_b128 v[204:207], v168
	v_add_u32_e32 v165, 0x18000, v163
	v_add_u32_e32 v163, 0x1c000, v163
	ds_read_b128 v[208:211], v165
	ds_read_b128 v[212:215], v163
	s_setprio 1
	s_waitcnt lgkmcnt(3)
	v_mfma_f32_16x16x32_f16 v[130:133], v[18:21], v[200:203], v[130:133]
	v_mfma_f32_16x16x32_f16 v[134:137], v[22:25], v[200:203], v[134:137]
	v_mfma_f32_16x16x32_f16 v[138:141], v[26:29], v[200:203], v[138:141]
	v_mfma_f32_16x16x32_f16 v[114:117], v[30:33], v[200:203], v[114:117]
	s_waitcnt lgkmcnt(2)
	v_mfma_f32_16x16x32_f16 v[142:145], v[18:21], v[204:207], v[142:145]
	v_mfma_f32_16x16x32_f16 v[146:149], v[22:25], v[204:207], v[146:149]
	v_mfma_f32_16x16x32_f16 v[150:153], v[26:29], v[204:207], v[150:153]
	v_mfma_f32_16x16x32_f16 v[118:121], v[30:33], v[204:207], v[118:121]
	s_waitcnt lgkmcnt(1)
	v_mfma_f32_16x16x32_f16 v[154:157], v[18:21], v[208:211], v[154:157]
	v_mfma_f32_16x16x32_f16 v[158:161], v[22:25], v[208:211], v[158:161]
	v_mfma_f32_16x16x32_f16 v[122:125], v[30:33], v[208:211], v[122:125]
	s_waitcnt lgkmcnt(0)
	v_mfma_f32_16x16x32_f16 v[2:5], v[18:21], v[212:215], v[2:5]
	v_mfma_f32_16x16x32_f16 v[6:9], v[22:25], v[212:215], v[6:9]
	v_mfma_f32_16x16x32_f16 v[10:13], v[26:29], v[212:215], v[10:13]
	v_mfma_f32_16x16x32_f16 v[14:17], v[30:33], v[212:215], v[14:17]
	v_mfma_f32_16x16x32_f16 v[170:173], v[26:29], v[208:211], v[170:173]
	s_setprio 0
	s_xor_b32 s25, s25, 4
	s_lshl_b32 s0, s25, 12
	v_lshl_add_u64 v[30:31], v[166:167], 0, s[0:1]
	s_waitcnt vmcnt(8)
	s_barrier
	s_getreg_b32 s80, hwreg(HW_REG_XCC_ID, 0, 4)
	s_and_b32 s80, s80, 15
	s_add_i32 s80, s80, 1
	s_lshl_b32 s81, s34, 3
	s_or_b32 s81, s81, s33
	s_lshl_b32 s81, s81, 7
	s_add_u32 s82, s46, s81
	s_addc_u32 s83, s47, 0
	v_mov_b32_e32 v254, 0
	v_mov_b32_e32 v255, s80
	s_and_saveexec_b64 s[84:85], s[4:5]
	global_store_dword v254, v255, s[82:83] sc1
	s_mov_b64 exec, s[84:85]
	global_load_dwordx4 v[18:21], v[30:31], off
	global_load_dwordx4 v[22:25], v[30:31], off offset:1024
	global_load_dwordx4 v[26:29], v[30:31], off offset:2048
	s_nop 0
	global_load_dwordx4 v[30:33], v[30:31], off offset:3072
	v_lshl_add_u32 v163, s31, 10, v191
	ds_read_b128 v[200:203], v163
	ds_read_b128 v[204:207], v163 offset:16384
	ds_read_b128 v[208:211], v163 offset:32768
	ds_read_b128 v[212:215], v163 offset:49152
	s_setprio 1
	s_waitcnt vmcnt(11) lgkmcnt(3)
	v_mfma_f32_16x16x32_f16 v[66:69], v[34:37], v[200:203], v[66:69]
	s_waitcnt vmcnt(10)
	v_mfma_f32_16x16x32_f16 v[70:73], v[38:41], v[200:203], v[70:73]
	s_waitcnt vmcnt(9)
	v_mfma_f32_16x16x32_f16 v[74:77], v[42:45], v[200:203], v[74:77]
	s_waitcnt vmcnt(8)
	v_mfma_f32_16x16x32_f16 v[50:53], v[46:49], v[200:203], v[50:53]
	s_waitcnt lgkmcnt(2)
	v_mfma_f32_16x16x32_f16 v[78:81], v[34:37], v[204:207], v[78:81]
	v_mfma_f32_16x16x32_f16 v[82:85], v[38:41], v[204:207], v[82:85]
	v_mfma_f32_16x16x32_f16 v[86:89], v[42:45], v[204:207], v[86:89]
	v_mfma_f32_16x16x32_f16 v[54:57], v[46:49], v[204:207], v[54:57]
	s_waitcnt lgkmcnt(1)
	v_mfma_f32_16x16x32_f16 v[90:93], v[34:37], v[208:211], v[90:93]
	v_mfma_f32_16x16x32_f16 v[94:97], v[38:41], v[208:211], v[94:97]
	v_mfma_f32_16x16x32_f16 v[98:101], v[42:45], v[208:211], v[98:101]
	v_mfma_f32_16x16x32_f16 v[58:61], v[46:49], v[208:211], v[58:61]
	s_waitcnt lgkmcnt(0)
	v_mfma_f32_16x16x32_f16 v[102:105], v[34:37], v[212:215], v[102:105]
	v_mfma_f32_16x16x32_f16 v[106:109], v[38:41], v[212:215], v[106:109]
	v_mfma_f32_16x16x32_f16 v[110:113], v[42:45], v[212:215], v[110:113]
	v_mfma_f32_16x16x32_f16 v[62:65], v[46:49], v[212:215], v[62:65]
	s_setprio 0
	v_add_u32_e32 v165, 0x10000, v163
	v_add_u32_e32 v168, 0x14000, v163
	ds_read_b128 v[200:203], v165
	ds_read_b128 v[204:207], v168
	v_add_u32_e32 v165, 0x18000, v163
	v_add_u32_e32 v163, 0x1c000, v163
	ds_read_b128 v[208:211], v165
	ds_read_b128 v[212:215], v163
	s_setprio 1
	s_waitcnt lgkmcnt(3)
	v_mfma_f32_16x16x32_f16 v[130:133], v[34:37], v[200:203], v[130:133]
	v_mfma_f32_16x16x32_f16 v[134:137], v[38:41], v[200:203], v[134:137]
	v_mfma_f32_16x16x32_f16 v[138:141], v[42:45], v[200:203], v[138:141]
	v_mfma_f32_16x16x32_f16 v[114:117], v[46:49], v[200:203], v[114:117]
	s_waitcnt lgkmcnt(2)
	v_mfma_f32_16x16x32_f16 v[142:145], v[34:37], v[204:207], v[142:145]
	v_mfma_f32_16x16x32_f16 v[146:149], v[38:41], v[204:207], v[146:149]
	v_mfma_f32_16x16x32_f16 v[150:153], v[42:45], v[204:207], v[150:153]
	v_mfma_f32_16x16x32_f16 v[118:121], v[46:49], v[204:207], v[118:121]
	s_waitcnt lgkmcnt(1)
	v_mfma_f32_16x16x32_f16 v[154:157], v[34:37], v[208:211], v[154:157]
	v_mfma_f32_16x16x32_f16 v[158:161], v[38:41], v[208:211], v[158:161]
	v_mfma_f32_16x16x32_f16 v[122:125], v[46:49], v[208:211], v[122:125]
	s_waitcnt lgkmcnt(0)
	v_mfma_f32_16x16x32_f16 v[2:5], v[34:37], v[212:215], v[2:5]
	v_mfma_f32_16x16x32_f16 v[6:9], v[38:41], v[212:215], v[6:9]
	v_mfma_f32_16x16x32_f16 v[10:13], v[42:45], v[212:215], v[10:13]
	v_mfma_f32_16x16x32_f16 v[14:17], v[46:49], v[212:215], v[14:17]
	v_mfma_f32_16x16x32_f16 v[170:173], v[42:45], v[208:211], v[170:173]
	s_setprio 0
	s_add_i32 s0, s50, 5
	s_and_b32 s30, s0, 7
	s_or_b32 s49, s30, s2
	s_lshl_b32 s0, s49, 12
	v_lshl_add_u64 v[46:47], v[166:167], 0, s[0:1]
	global_load_dwordx4 v[34:37], v[46:47], off
	global_load_dwordx4 v[38:41], v[46:47], off offset:1024
	global_load_dwordx4 v[42:45], v[46:47], off offset:2048
	s_nop 0
	global_load_dwordx4 v[46:49], v[46:47], off offset:3072
	v_lshl_add_u32 v163, s48, 10, v191
	ds_read_b128 v[200:203], v163
	ds_read_b128 v[204:207], v163 offset:16384
	ds_read_b128 v[208:211], v163 offset:32768
	ds_read_b128 v[212:215], v163 offset:49152
	s_setprio 1
	s_waitcnt vmcnt(11) lgkmcnt(3)
	v_mfma_f32_16x16x32_f16 v[66:69], v[126:129], v[200:203], v[66:69]
	s_waitcnt vmcnt(10)
	v_mfma_f32_16x16x32_f16 v[70:73], v[174:177], v[200:203], v[70:73]
	s_waitcnt vmcnt(9)
	v_mfma_f32_16x16x32_f16 v[74:77], v[192:195], v[200:203], v[74:77]
	s_waitcnt vmcnt(8)
	v_mfma_f32_16x16x32_f16 v[50:53], v[196:199], v[200:203], v[50:53]
	s_waitcnt lgkmcnt(2)
	v_mfma_f32_16x16x32_f16 v[78:81], v[126:129], v[204:207], v[78:81]
	v_mfma_f32_16x16x32_f16 v[82:85], v[174:177], v[204:207], v[82:85]
	v_mfma_f32_16x16x32_f16 v[86:89], v[192:195], v[204:207], v[86:89]
	v_mfma_f32_16x16x32_f16 v[54:57], v[196:199], v[204:207], v[54:57]
	s_waitcnt lgkmcnt(1)
	v_mfma_f32_16x16x32_f16 v[90:93], v[126:129], v[208:211], v[90:93]
	v_mfma_f32_16x16x32_f16 v[94:97], v[174:177], v[208:211], v[94:97]
	v_mfma_f32_16x16x32_f16 v[98:101], v[192:195], v[208:211], v[98:101]
	v_mfma_f32_16x16x32_f16 v[58:61], v[196:199], v[208:211], v[58:61]
	s_waitcnt lgkmcnt(0)
	v_mfma_f32_16x16x32_f16 v[102:105], v[126:129], v[212:215], v[102:105]
	v_mfma_f32_16x16x32_f16 v[106:109], v[174:177], v[212:215], v[106:109]
	v_mfma_f32_16x16x32_f16 v[110:113], v[192:195], v[212:215], v[110:113]
	v_mfma_f32_16x16x32_f16 v[62:65], v[196:199], v[212:215], v[62:65]
	s_setprio 0
	v_add_u32_e32 v165, 0x10000, v163
	v_add_u32_e32 v168, 0x14000, v163
	ds_read_b128 v[200:203], v165
	ds_read_b128 v[204:207], v168
	v_add_u32_e32 v165, 0x18000, v163
	v_add_u32_e32 v163, 0x1c000, v163
	ds_read_b128 v[208:211], v165
	ds_read_b128 v[212:215], v163
	s_setprio 1
	s_waitcnt lgkmcnt(3)
	v_mfma_f32_16x16x32_f16 v[130:133], v[126:129], v[200:203], v[130:133]
	v_mfma_f32_16x16x32_f16 v[134:137], v[174:177], v[200:203], v[134:137]
	v_mfma_f32_16x16x32_f16 v[138:141], v[192:195], v[200:203], v[138:141]
	v_mfma_f32_16x16x32_f16 v[114:117], v[196:199], v[200:203], v[114:117]
	s_waitcnt lgkmcnt(2)
	v_mfma_f32_16x16x32_f16 v[142:145], v[126:129], v[204:207], v[142:145]
	v_mfma_f32_16x16x32_f16 v[146:149], v[174:177], v[204:207], v[146:149]
	v_mfma_f32_16x16x32_f16 v[150:153], v[192:195], v[204:207], v[150:153]
	v_mfma_f32_16x16x32_f16 v[118:121], v[196:199], v[204:207], v[118:121]
	s_waitcnt lgkmcnt(1)
	v_mfma_f32_16x16x32_f16 v[154:157], v[126:129], v[208:211], v[154:157]
	v_mfma_f32_16x16x32_f16 v[158:161], v[174:177], v[208:211], v[158:161]
	v_mfma_f32_16x16x32_f16 v[122:125], v[196:199], v[208:211], v[122:125]
	s_waitcnt lgkmcnt(0)
	v_mfma_f32_16x16x32_f16 v[2:5], v[126:129], v[212:215], v[2:5]
	v_mfma_f32_16x16x32_f16 v[6:9], v[174:177], v[212:215], v[6:9]
	v_mfma_f32_16x16x32_f16 v[10:13], v[192:195], v[212:215], v[10:13]
	v_mfma_f32_16x16x32_f16 v[14:17], v[196:199], v[212:215], v[14:17]
	v_mfma_f32_16x16x32_f16 v[170:173], v[192:195], v[208:211], v[170:173]
	s_setprio 0
	s_add_i32 s59, s59, 6
	s_and_b32 s31, s59, 6
	s_or_b32 s52, s2, s31
	s_lshl_b32 s0, s52, 12
	v_lshl_add_u64 v[178:179], v[166:167], 0, s[0:1]
	s_lshl_b32 s86, s34, 3
	s_or_b32 s86, s86, s33
	s_xor_b32 s86, s86, 1
	s_lshl_b32 s86, s86, 7
	s_add_u32 s86, s46, s86
	s_addc_u32 s87, s47, 0
	v_mov_b32_e32 v254, 0
	global_load_dword v254, v254, s[86:87] sc1
	global_load_dwordx4 v[126:129], v[178:179], off
	global_load_dwordx4 v[174:177], v[178:179], off offset:1024
	global_load_dwordx4 v[192:195], v[178:179], off offset:2048
	global_load_dwordx4 v[196:199], v[178:179], off offset:3072
	v_lshl_add_u32 v163, s25, 10, v191
	ds_read_b128 v[200:203], v163
	ds_read_b128 v[204:207], v163 offset:16384
	ds_read_b128 v[208:211], v163 offset:32768
	ds_read_b128 v[212:215], v163 offset:49152
	s_setprio 1
	s_waitcnt vmcnt(12) lgkmcnt(3)
	v_mfma_f32_16x16x32_f16 v[66:69], v[18:21], v[200:203], v[66:69]
	s_waitcnt vmcnt(11)
	v_mfma_f32_16x16x32_f16 v[70:73], v[22:25], v[200:203], v[70:73]
	s_waitcnt vmcnt(10)
	v_mfma_f32_16x16x32_f16 v[74:77], v[26:29], v[200:203], v[74:77]
	s_waitcnt vmcnt(9)
	v_mfma_f32_16x16x32_f16 v[50:53], v[30:33], v[200:203], v[50:53]
	s_waitcnt lgkmcnt(2)
	v_mfma_f32_16x16x32_f16 v[78:81], v[18:21], v[204:207], v[78:81]
	v_mfma_f32_16x16x32_f16 v[82:85], v[22:25], v[204:207], v[82:85]
	v_mfma_f32_16x16x32_f16 v[86:89], v[26:29], v[204:207], v[86:89]
	v_mfma_f32_16x16x32_f16 v[54:57], v[30:33], v[204:207], v[54:57]
	s_waitcnt lgkmcnt(1)
	v_mfma_f32_16x16x32_f16 v[90:93], v[18:21], v[208:211], v[90:93]
	v_mfma_f32_16x16x32_f16 v[94:97], v[22:25], v[208:211], v[94:97]
	v_mfma_f32_16x16x32_f16 v[98:101], v[26:29], v[208:211], v[98:101]
	v_mfma_f32_16x16x32_f16 v[58:61], v[30:33], v[208:211], v[58:61]
	s_waitcnt lgkmcnt(0)
	v_mfma_f32_16x16x32_f16 v[102:105], v[18:21], v[212:215], v[102:105]
	v_mfma_f32_16x16x32_f16 v[106:109], v[22:25], v[212:215], v[106:109]
	v_mfma_f32_16x16x32_f16 v[110:113], v[26:29], v[212:215], v[110:113]
	v_mfma_f32_16x16x32_f16 v[62:65], v[30:33], v[212:215], v[62:65]
	s_setprio 0
	v_add_u32_e32 v165, 0x10000, v163
	v_add_u32_e32 v168, 0x14000, v163
	ds_read_b128 v[200:203], v165
	ds_read_b128 v[204:207], v168
	v_add_u32_e32 v165, 0x18000, v163
	v_add_u32_e32 v163, 0x1c000, v163
	ds_read_b128 v[208:211], v165
	ds_read_b128 v[212:215], v163
	s_setprio 1
	s_waitcnt lgkmcnt(3)
	v_mfma_f32_16x16x32_f16 v[130:133], v[18:21], v[200:203], v[130:133]
	v_mfma_f32_16x16x32_f16 v[134:137], v[22:25], v[200:203], v[134:137]
	v_mfma_f32_16x16x32_f16 v[138:141], v[26:29], v[200:203], v[138:141]
	v_mfma_f32_16x16x32_f16 v[114:117], v[30:33], v[200:203], v[114:117]
	s_waitcnt lgkmcnt(2)
	v_mfma_f32_16x16x32_f16 v[142:145], v[18:21], v[204:207], v[142:145]
	v_mfma_f32_16x16x32_f16 v[146:149], v[22:25], v[204:207], v[146:149]
	v_mfma_f32_16x16x32_f16 v[150:153], v[26:29], v[204:207], v[150:153]
	v_mfma_f32_16x16x32_f16 v[118:121], v[30:33], v[204:207], v[118:121]
	s_waitcnt lgkmcnt(1)
	v_mfma_f32_16x16x32_f16 v[154:157], v[18:21], v[208:211], v[154:157]
	v_mfma_f32_16x16x32_f16 v[158:161], v[22:25], v[208:211], v[158:161]
	v_mfma_f32_16x16x32_f16 v[122:125], v[30:33], v[208:211], v[122:125]
	s_waitcnt lgkmcnt(0)
	v_mfma_f32_16x16x32_f16 v[2:5], v[18:21], v[212:215], v[2:5]
	v_mfma_f32_16x16x32_f16 v[6:9], v[22:25], v[212:215], v[6:9]
	v_mfma_f32_16x16x32_f16 v[10:13], v[26:29], v[212:215], v[10:13]
	v_mfma_f32_16x16x32_f16 v[14:17], v[30:33], v[212:215], v[14:17]
	v_mfma_f32_16x16x32_f16 v[170:173], v[26:29], v[208:211], v[170:173]
	s_setprio 0
	s_add_i32 s0, s50, -1
	s_and_b32 s48, s0, 7
	s_or_b32 s25, s48, s2
	s_lshl_b32 s0, s25, 12
	v_lshl_add_u64 v[18:19], v[166:167], 0, s[0:1]
	global_load_dwordx4 v[200:203], v[18:19], off
	global_load_dwordx4 v[204:207], v[18:19], off offset:1024
	global_load_dwordx4 v[208:211], v[18:19], off offset:2048
	global_load_dwordx4 v[212:215], v[18:19], off offset:3072
	v_lshl_add_u32 v163, s49, 10, v191
	ds_read_b128 v[18:21], v163
	ds_read_b128 v[22:25], v163 offset:16384
	ds_read_b128 v[26:29], v163 offset:32768
	ds_read_b128 v[30:33], v163 offset:49152
	s_setprio 1
	s_waitcnt vmcnt(12) lgkmcnt(3)
	v_mfma_f32_16x16x32_f16 v[66:69], v[34:37], v[18:21], v[66:69]
	s_waitcnt vmcnt(11)
	v_mfma_f32_16x16x32_f16 v[70:73], v[38:41], v[18:21], v[70:73]
	s_waitcnt vmcnt(10)
	v_mfma_f32_16x16x32_f16 v[74:77], v[42:45], v[18:21], v[74:77]
	s_waitcnt vmcnt(9)
	v_mfma_f32_16x16x32_f16 v[18:21], v[46:49], v[18:21], v[50:53]
	s_waitcnt lgkmcnt(2)
	v_mfma_f32_16x16x32_f16 v[50:53], v[34:37], v[22:25], v[78:81]
	v_mfma_f32_16x16x32_f16 v[78:81], v[38:41], v[22:25], v[82:85]
	v_mfma_f32_16x16x32_f16 v[82:85], v[42:45], v[22:25], v[86:89]
	v_mfma_f32_16x16x32_f16 v[22:25], v[46:49], v[22:25], v[54:57]
	s_waitcnt lgkmcnt(1)
	v_mfma_f32_16x16x32_f16 v[54:57], v[34:37], v[26:29], v[90:93]
	v_mfma_f32_16x16x32_f16 v[86:89], v[38:41], v[26:29], v[94:97]
	v_mfma_f32_16x16x32_f16 v[90:93], v[42:45], v[26:29], v[98:101]
	v_mfma_f32_16x16x32_f16 v[26:29], v[46:49], v[26:29], v[58:61]
	s_waitcnt lgkmcnt(0)
	v_mfma_f32_16x16x32_f16 v[58:61], v[34:37], v[30:33], v[102:105]
	v_mfma_f32_16x16x32_f16 v[94:97], v[38:41], v[30:33], v[106:109]
	v_mfma_f32_16x16x32_f16 v[98:101], v[42:45], v[30:33], v[110:113]
	v_mfma_f32_16x16x32_f16 v[30:33], v[46:49], v[30:33], v[62:65]
	s_setprio 0
	s_nop 1
	v_add_u32_e32 v62, 0x10000, v163
	v_add_u32_e32 v102, 0x14000, v163
	v_add_u32_e32 v106, 0x18000, v163
	v_add_u32_e32 v110, 0x1c000, v163
	ds_read_b128 v[62:65], v62
	ds_read_b128 v[102:105], v102
	ds_read_b128 v[106:109], v106
	ds_read_b128 v[110:113], v110
	s_setprio 1
	s_waitcnt lgkmcnt(3)
	v_mfma_f32_16x16x32_f16 v[130:133], v[34:37], v[62:65], v[130:133]
	v_mfma_f32_16x16x32_f16 v[134:137], v[38:41], v[62:65], v[134:137]
	v_mfma_f32_16x16x32_f16 v[138:141], v[42:45], v[62:65], v[138:141]
	v_mfma_f32_16x16x32_f16 v[62:65], v[46:49], v[62:65], v[114:117]
	s_waitcnt lgkmcnt(2)
	v_mfma_f32_16x16x32_f16 v[114:117], v[34:37], v[102:105], v[142:145]
	v_mfma_f32_16x16x32_f16 v[142:145], v[38:41], v[102:105], v[146:149]
	v_mfma_f32_16x16x32_f16 v[146:149], v[42:45], v[102:105], v[150:153]
	v_mfma_f32_16x16x32_f16 v[102:105], v[46:49], v[102:105], v[118:121]
	s_waitcnt lgkmcnt(1)
	v_mfma_f32_16x16x32_f16 v[118:121], v[34:37], v[106:109], v[154:157]
	v_mfma_f32_16x16x32_f16 v[150:153], v[38:41], v[106:109], v[158:161]
	v_mfma_f32_16x16x32_f16 v[154:157], v[42:45], v[106:109], v[170:173]
	v_mfma_f32_16x16x32_f16 v[106:109], v[46:49], v[106:109], v[122:125]
	s_waitcnt lgkmcnt(0)
	v_mfma_f32_16x16x32_f16 v[34:37], v[34:37], v[110:113], v[2:5]
	v_mfma_f32_16x16x32_f16 v[38:41], v[38:41], v[110:113], v[6:9]
	v_mfma_f32_16x16x32_f16 v[42:45], v[42:45], v[110:113], v[10:13]
	v_mfma_f32_16x16x32_f16 v[46:49], v[46:49], v[110:113], v[14:17]
	s_setprio 0
	s_xor_b32 s2, s58, 1
	s_lshl_b32 s49, s2, 3
	s_or_b32 s51, s49, s50
	s_lshl_b32 s0, s51, 12
	v_lshl_add_u64 v[14:15], v[166:167], 0, s[0:1]
	s_waitcnt vmcnt(8)
	s_barrier
	v_lshlrev_b32_e32 v255, 4, v0
	v_readfirstlane_b32 s92, v0
	s_lshl_b32 s92, s92, 4
	s_xor_b32 s93, s58, 1
	s_lshl_b32 s94, s93, 13
	s_add_i32 s92, s92, s94
	s_lshl_b32 s94, s34, 3
	s_or_b32 s94, s94, s33
	s_xor_b32 s94, s94, 1
	s_lshl_b32 s94, s94, 16
	s_add_u32 s88, s26, s94
	s_addc_u32 s89, s27, 0
	s_add_i32 s95, s92, 0x0
	s_mov_b32 m0, s95
	s_add_u32 s84, s88, 0x0
	s_addc_u32 s85, s89, 0
	global_load_lds_dwordx4 v255, s[84:85] sc0 sc1
	s_add_i32 s95, s92, 0x4000
	s_mov_b32 m0, s95
	s_add_u32 s84, s88, 0x2000
	s_addc_u32 s85, s89, 0
	global_load_lds_dwordx4 v255, s[84:85] sc0 sc1
	s_add_i32 s95, s92, 0x8000
	s_mov_b32 m0, s95
	s_add_u32 s84, s88, 0x4000
	s_addc_u32 s85, s89, 0
	global_load_lds_dwordx4 v255, s[84:85] sc0 sc1
	s_add_i32 s95, s92, 0xc000
	s_mov_b32 m0, s95
	s_add_u32 s84, s88, 0x6000
	s_addc_u32 s85, s89, 0
	global_load_lds_dwordx4 v255, s[84:85] sc0 sc1
	s_add_i32 s95, s92, 0x10000
	s_mov_b32 m0, s95
	s_add_u32 s84, s88, 0x8000
	s_addc_u32 s85, s89, 0
	global_load_lds_dwordx4 v255, s[84:85] sc0 sc1
	s_add_i32 s95, s92, 0x14000
	s_mov_b32 m0, s95
	s_add_u32 s84, s88, 0xa000
	s_addc_u32 s85, s89, 0
	global_load_lds_dwordx4 v255, s[84:85] sc0 sc1
	s_add_i32 s95, s92, 0x18000
	s_mov_b32 m0, s95
	s_add_u32 s84, s88, 0xc000
	s_addc_u32 s85, s89, 0
	global_load_lds_dwordx4 v255, s[84:85] sc0 sc1
	s_add_i32 s95, s92, 0x1c000
	s_mov_b32 m0, s95
	s_add_u32 s84, s88, 0xe000
	s_addc_u32 s85, s89, 0
	global_load_lds_dwordx4 v255, s[84:85] sc0 sc1
	global_load_dwordx4 v[2:5], v[14:15], off
	global_load_dwordx4 v[6:9], v[14:15], off offset:1024
	global_load_dwordx4 v[10:13], v[14:15], off offset:2048
	s_nop 0
	global_load_dwordx4 v[14:17], v[14:15], off offset:3072
	v_lshl_add_u32 v163, s52, 10, v191
	ds_read_b128 v[110:113], v163
	ds_read_b128 v[122:125], v163 offset:16384
	ds_read_b128 v[158:161], v163 offset:32768
	ds_read_b128 v[170:173], v163 offset:49152
	s_setprio 1
	s_waitcnt vmcnt(19) lgkmcnt(3)
	v_mfma_f32_16x16x32_f16 v[66:69], v[126:129], v[110:113], v[66:69]
	s_waitcnt vmcnt(18)
	v_mfma_f32_16x16x32_f16 v[70:73], v[174:177], v[110:113], v[70:73]
	s_waitcnt vmcnt(17)
	v_mfma_f32_16x16x32_f16 v[74:77], v[192:195], v[110:113], v[74:77]
	s_waitcnt vmcnt(16)
	v_mfma_f32_16x16x32_f16 v[110:113], v[196:199], v[110:113], v[18:21]
	s_waitcnt lgkmcnt(2)
	v_mfma_f32_16x16x32_f16 v[50:53], v[126:129], v[122:125], v[50:53]
	v_mfma_f32_16x16x32_f16 v[78:81], v[174:177], v[122:125], v[78:81]
	v_mfma_f32_16x16x32_f16 v[82:85], v[192:195], v[122:125], v[82:85]
	v_mfma_f32_16x16x32_f16 v[122:125], v[196:199], v[122:125], v[22:25]
	s_waitcnt lgkmcnt(1)
	v_mfma_f32_16x16x32_f16 v[216:219], v[126:129], v[158:161], v[54:57]
	v_mfma_f32_16x16x32_f16 v[86:89], v[174:177], v[158:161], v[86:89]
	v_mfma_f32_16x16x32_f16 v[90:93], v[192:195], v[158:161], v[90:93]
	v_mfma_f32_16x16x32_f16 v[158:161], v[196:199], v[158:161], v[26:29]
	s_waitcnt lgkmcnt(0)
	v_mfma_f32_16x16x32_f16 v[94:97], v[174:177], v[170:173], v[94:97]
	v_mfma_f32_16x16x32_f16 v[98:101], v[192:195], v[170:173], v[98:101]
	v_mfma_f32_16x16x32_f16 v[220:223], v[126:129], v[170:173], v[58:61]
	v_mfma_f32_16x16x32_f16 v[170:173], v[196:199], v[170:173], v[30:33]
	s_setprio 0
	v_add_u32_e32 v18, 0x10000, v163
	v_add_u32_e32 v22, 0x14000, v163
	v_add_u32_e32 v26, 0x18000, v163
	v_add_u32_e32 v30, 0x1c000, v163
	ds_read_b128 v[18:21], v18
	ds_read_b128 v[22:25], v22
	ds_read_b128 v[26:29], v26
	ds_read_b128 v[30:33], v30
	s_setprio 1
	s_waitcnt lgkmcnt(3)
	v_mfma_f32_16x16x32_f16 v[130:133], v[126:129], v[18:21], v[130:133]
	v_mfma_f32_16x16x32_f16 v[134:137], v[174:177], v[18:21], v[134:137]
	v_mfma_f32_16x16x32_f16 v[138:141], v[192:195], v[18:21], v[138:141]
	s_waitcnt lgkmcnt(2)
	v_mfma_f32_16x16x32_f16 v[114:117], v[126:129], v[22:25], v[114:117]
	v_mfma_f32_16x16x32_f16 v[142:145], v[174:177], v[22:25], v[142:145]
	v_mfma_f32_16x16x32_f16 v[146:149], v[192:195], v[22:25], v[146:149]
	s_waitcnt lgkmcnt(1)
	v_mfma_f32_16x16x32_f16 v[150:153], v[174:177], v[26:29], v[150:153]
	v_mfma_f32_16x16x32_f16 v[154:157], v[192:195], v[26:29], v[154:157]
	v_mfma_f32_16x16x32_f16 v[224:227], v[196:199], v[18:21], v[62:65]
	v_mfma_f32_16x16x32_f16 v[228:231], v[196:199], v[22:25], v[102:105]
	v_mfma_f32_16x16x32_f16 v[232:235], v[126:129], v[26:29], v[118:121]
	v_mfma_f32_16x16x32_f16 v[236:239], v[196:199], v[26:29], v[106:109]
	s_waitcnt lgkmcnt(0)
	v_mfma_f32_16x16x32_f16 v[240:243], v[126:129], v[30:33], v[34:37]
	v_mfma_f32_16x16x32_f16 v[174:177], v[174:177], v[30:33], v[38:41]
	v_mfma_f32_16x16x32_f16 v[192:195], v[192:195], v[30:33], v[42:45]
	v_mfma_f32_16x16x32_f16 v[196:199], v[196:199], v[30:33], v[46:49]
	s_setprio 0
	s_or_b32 s52, s49, s24
	s_lshl_b32 s0, s52, 12
	v_lshl_add_u64 v[30:31], v[166:167], 0, s[0:1]
	global_load_dwordx4 v[18:21], v[30:31], off
	global_load_dwordx4 v[22:25], v[30:31], off offset:1024
	global_load_dwordx4 v[26:29], v[30:31], off offset:2048
	s_nop 0
	global_load_dwordx4 v[30:33], v[30:31], off offset:3072
	v_lshl_add_u32 v118, s25, 10, v191
	ds_read_b128 v[46:49], v118
	ds_read_b128 v[62:65], v118 offset:16384
	ds_read_b128 v[102:105], v118 offset:32768
	ds_read_b128 v[106:109], v118 offset:49152
	s_setprio 1
	s_waitcnt vmcnt(19) lgkmcnt(3)
	v_mfma_f32_16x16x32_f16 v[34:37], v[200:203], v[46:49], v[66:69]
	s_waitcnt vmcnt(18)
	v_mfma_f32_16x16x32_f16 v[38:41], v[204:207], v[46:49], v[70:73]
	s_waitcnt vmcnt(17)
	v_mfma_f32_16x16x32_f16 v[42:45], v[208:211], v[46:49], v[74:77]
	s_waitcnt vmcnt(16)
	v_mfma_f32_16x16x32_f16 v[46:49], v[212:215], v[46:49], v[110:113]
	s_waitcnt lgkmcnt(2)
	v_mfma_f32_16x16x32_f16 v[50:53], v[200:203], v[62:65], v[50:53]
	v_mfma_f32_16x16x32_f16 v[54:57], v[204:207], v[62:65], v[78:81]
	v_mfma_f32_16x16x32_f16 v[58:61], v[208:211], v[62:65], v[82:85]
	v_mfma_f32_16x16x32_f16 v[62:65], v[212:215], v[62:65], v[122:125]
	s_waitcnt lgkmcnt(1)
	v_mfma_f32_16x16x32_f16 v[66:69], v[200:203], v[102:105], v[216:219]
	v_mfma_f32_16x16x32_f16 v[70:73], v[204:207], v[102:105], v[86:89]
	v_mfma_f32_16x16x32_f16 v[74:77], v[208:211], v[102:105], v[90:93]
	v_mfma_f32_16x16x32_f16 v[78:81], v[212:215], v[102:105], v[158:161]
	s_waitcnt lgkmcnt(0)
	v_mfma_f32_16x16x32_f16 v[82:85], v[200:203], v[106:109], v[220:223]
	v_mfma_f32_16x16x32_f16 v[86:89], v[204:207], v[106:109], v[94:97]
	v_mfma_f32_16x16x32_f16 v[90:93], v[208:211], v[106:109], v[98:101]
	v_mfma_f32_16x16x32_f16 v[94:97], v[212:215], v[106:109], v[170:173]
	s_setprio 0
	s_nop 0
	v_add_u32_e32 v98, 0x10000, v118
	v_add_u32_e32 v99, 0x14000, v118
	ds_read_b128 v[110:113], v98
	ds_read_b128 v[126:129], v99
	v_add_u32_e32 v98, 0x18000, v118
	v_add_u32_e32 v99, 0x1c000, v118
	ds_read_b128 v[158:161], v98
	ds_read_b128 v[170:173], v99
	s_setprio 1
	s_waitcnt lgkmcnt(3)
	v_mfma_f32_16x16x32_f16 v[98:101], v[200:203], v[110:113], v[130:133]
	v_mfma_f32_16x16x32_f16 v[102:105], v[204:207], v[110:113], v[134:137]
	v_mfma_f32_16x16x32_f16 v[106:109], v[208:211], v[110:113], v[138:141]
	v_mfma_f32_16x16x32_f16 v[110:113], v[212:215], v[110:113], v[224:227]
	s_waitcnt lgkmcnt(2)
	v_mfma_f32_16x16x32_f16 v[114:117], v[200:203], v[126:129], v[114:117]
	v_mfma_f32_16x16x32_f16 v[118:121], v[204:207], v[126:129], v[142:145]
	v_mfma_f32_16x16x32_f16 v[122:125], v[208:211], v[126:129], v[146:149]
	v_mfma_f32_16x16x32_f16 v[126:129], v[212:215], v[126:129], v[228:231]
	s_waitcnt lgkmcnt(1)
	v_mfma_f32_16x16x32_f16 v[130:133], v[200:203], v[158:161], v[232:235]
	v_mfma_f32_16x16x32_f16 v[134:137], v[204:207], v[158:161], v[150:153]
	v_mfma_f32_16x16x32_f16 v[138:141], v[208:211], v[158:161], v[154:157]
	v_mfma_f32_16x16x32_f16 v[142:145], v[212:215], v[158:161], v[236:239]
	s_waitcnt lgkmcnt(0)
	v_mfma_f32_16x16x32_f16 v[146:149], v[200:203], v[170:173], v[240:243]
	v_mfma_f32_16x16x32_f16 v[150:153], v[204:207], v[170:173], v[174:177]
	v_mfma_f32_16x16x32_f16 v[154:157], v[208:211], v[170:173], v[192:195]
	v_mfma_f32_16x16x32_f16 v[158:161], v[212:215], v[170:173], v[196:199]
	s_setprio 0
	s_waitcnt vmcnt(0)
	s_barrier
	s_getreg_b32 s24, hwreg(HW_REG_XCC_ID, 0, 4)
	s_and_saveexec_b64 s[0:1], s[4:5]
	s_cbranch_execz .LBB5_145
	s_and_b32 s53, s24, 15
	s_lshl_b32 s24, s34, 3
	s_or_b32 s50, s24, s50
	s_or_b32 s24, s50, s58
	s_lshl_b32 s24, s24, 5
	s_ashr_i32 s25, s24, 31
	s_lshl_b64 s[24:25], s[24:25], 2
	s_add_u32 s24, s46, s24
	s_addc_u32 s25, s47, s25
	s_add_i32 s54, s53, 1
	v_mov_b32_e32 v163, s54
	s_or_b32 s24, s50, s2
	s_lshl_b32 s24, s24, 5
	s_ashr_i32 s25, s24, 31
	s_lshl_b64 s[24:25], s[24:25], 2
	s_add_u32 s24, s46, s24
	s_addc_u32 s25, s47, s25
	s_mov_b32 s90, 0
	v_mov_b32_e32 v163, v254
	v_cmp_ne_u32_e32 vcc, 0, v163
	s_cbranch_vccnz .LBB5_144
	s_mov_b32 s90, 2
	v_mov_b32_e32 v165, 0
